# score loop: packed f32 fma/add replaced by scalar VALU; final rmsnorm pass: final_g loads hoisted and issued together with counted waits
# speedup vs baseline: 1.0031x; 1.0031x over previous
.LBB0_390:
	s_cmp_lt_i32 s30, 5
	s_cselect_b64 s[6:7], -1, 0
	s_add_u32 s52, s50, 0x5f7d0000
	s_addc_u32 s53, s51, 0
	s_and_b64 s[8:9], s[6:7], s[0:1]
	s_andn2_b64 vcc, exec, s[8:9]
	s_cbranch_vccnz .LBB0_446
	s_lshl_b32 s18, s2, 9
	s_waitcnt vmcnt(0)
	v_or_b32_e32 v2, s18, v0
	s_mov_b32 s0, 0x20000
	v_cmp_gt_i32_e32 vcc, s0, v2
	s_and_saveexec_b64 s[0:1], vcc
	s_cbranch_execz .LBB0_396
	s_lshl_b32 s6, s28, 9
	v_and_b32_e32 v1, 0x7f, v0
	v_ashrrev_i32_e32 v3, 31, v2
	s_ashr_i32 s7, s6, 31
	v_lshlrev_b64 v[4:5], 1, v[2:3]
	s_lshl_b64 s[10:11], s[6:7], 1
	v_lshlrev_b32_e32 v6, 2, v1
	s_mov_b64 s[12:13], 0
	s_movk_i32 s3, 0x7fff
	s_mov_b64 s[14:15], 0x400000
	s_mov_b64 s[16:17], 0x10000
	s_mov_b32 s7, 0x1ffff
.LBB0_393:
	v_ashrrev_i32_e32 v1, 7, v2
	v_and_b32_e32 v8, 0xffffff80, v1
	v_ashrrev_i32_e32 v9, 31, v8
	v_lshlrev_b64 v[8:9], 2, v[8:9]
	v_or_b32_e32 v8, v6, v8
	s_mov_b32 s19, -16
	v_mov_b64_e32 v[10:11], v[4:5]
	v_mov_b32_e32 v1, 0
.LBB0_394:
	v_lshl_add_u64 v[12:13], s[50:51], 0, v[10:11]
	v_add_co_u32_e32 v16, vcc, 0x4e6d0000, v12
	v_lshl_add_u64 v[14:15], s[50:51], 0, v[8:9]
	s_nop 0
	v_addc_co_u32_e32 v17, vcc, 0, v13, vcc
	v_add_co_u32_e32 v18, vcc, 0x566d0000, v14
	v_bfe_u32 v3, v1, 16, 1
	s_nop 0
	v_addc_co_u32_e32 v19, vcc, 0, v15, vcc
	v_add_co_u32_e32 v20, vcc, 0x4e710000, v12
	global_load_ushort v7, v[16:17], off
	global_load_dword v50, v[18:19], off
	v_addc_co_u32_e32 v21, vcc, 0, v13, vcc
	v_add_co_u32_e32 v18, vcc, 0x566d1000, v14
	v_add3_u32 v3, v1, v3, s3
	s_nop 0
	v_addc_co_u32_e32 v19, vcc, 0, v15, vcc
	v_add_co_u32_e32 v22, vcc, 0x4e750000, v12
	global_load_ushort v51, v[20:21], off
	global_load_dword v52, v[18:19], off
	v_addc_co_u32_e32 v23, vcc, 0, v13, vcc
	v_add_co_u32_e32 v18, vcc, 0x566d2000, v14
	s_add_i32 s19, s19, 16
	s_nop 0
	v_addc_co_u32_e32 v19, vcc, 0, v15, vcc
	v_add_co_u32_e32 v24, vcc, 0x4e790000, v12
	global_load_ushort v53, v[22:23], off
	global_load_dword v54, v[18:19], off
	v_addc_co_u32_e32 v25, vcc, 0, v13, vcc
	v_add_co_u32_e32 v18, vcc, 0x566d3000, v14
	v_lshl_add_u64 v[10:11], v[10:11], 0, s[14:15]
	s_nop 0
	v_addc_co_u32_e32 v19, vcc, 0, v15, vcc
	v_add_co_u32_e32 v26, vcc, 0x4e7d0000, v12
	global_load_ushort v55, v[24:25], off
	global_load_dword v56, v[18:19], off
	v_addc_co_u32_e32 v27, vcc, 0, v13, vcc
	v_add_co_u32_e32 v18, vcc, 0x566d4000, v14
	v_lshl_add_u64 v[8:9], v[8:9], 0, s[16:17]
	s_nop 0
	v_addc_co_u32_e32 v19, vcc, 0, v15, vcc
	v_add_co_u32_e32 v28, vcc, 0x4e810000, v12
	global_load_ushort v57, v[26:27], off
	global_load_dword v58, v[18:19], off
	v_addc_co_u32_e32 v29, vcc, 0, v13, vcc
	v_add_co_u32_e32 v18, vcc, 0x566d5000, v14
	s_cmpk_gt_u32 s19, 0xef
	s_nop 0
	v_addc_co_u32_e32 v19, vcc, 0, v15, vcc
	v_add_co_u32_e32 v30, vcc, 0x4e850000, v12
	global_load_ushort v59, v[28:29], off
	global_load_dword v60, v[18:19], off
	v_addc_co_u32_e32 v31, vcc, 0, v13, vcc
	v_add_co_u32_e32 v18, vcc, 0x566d6000, v14
	s_nop 1
	v_addc_co_u32_e32 v19, vcc, 0, v15, vcc
	v_add_co_u32_e32 v32, vcc, 0x4e890000, v12
	global_load_ushort v61, v[30:31], off
	global_load_dword v62, v[18:19], off
	v_addc_co_u32_e32 v33, vcc, 0, v13, vcc
	v_add_co_u32_e32 v18, vcc, 0x566d7000, v14
	s_nop 1
	v_addc_co_u32_e32 v19, vcc, 0, v15, vcc
	v_add_co_u32_e32 v34, vcc, 0x4e8d0000, v12
	global_load_ushort v63, v[32:33], off
	global_load_dword v64, v[18:19], off
	v_addc_co_u32_e32 v35, vcc, 0, v13, vcc
	v_add_co_u32_e32 v18, vcc, 0x566d8000, v14
	s_nop 1
	v_addc_co_u32_e32 v19, vcc, 0, v15, vcc
	v_add_co_u32_e32 v36, vcc, 0x4e910000, v12
	global_load_ushort v65, v[34:35], off
	global_load_dword v66, v[18:19], off
	v_addc_co_u32_e32 v37, vcc, 0, v13, vcc
	v_add_co_u32_e32 v18, vcc, 0x566d9000, v14
	s_nop 1
	v_addc_co_u32_e32 v19, vcc, 0, v15, vcc
	v_add_co_u32_e32 v38, vcc, 0x4e950000, v12
	global_load_ushort v67, v[36:37], off
	global_load_dword v68, v[18:19], off
	v_addc_co_u32_e32 v39, vcc, 0, v13, vcc
	v_add_co_u32_e32 v18, vcc, 0x566da000, v14
	s_nop 1
	v_addc_co_u32_e32 v19, vcc, 0, v15, vcc
	v_add_co_u32_e32 v40, vcc, 0x4e990000, v12
	global_load_ushort v69, v[38:39], off
	global_load_dword v70, v[18:19], off
	v_addc_co_u32_e32 v41, vcc, 0, v13, vcc
	v_add_co_u32_e32 v18, vcc, 0x566db000, v14
	s_nop 1
	v_addc_co_u32_e32 v19, vcc, 0, v15, vcc
	v_add_co_u32_e32 v42, vcc, 0x4e9d0000, v12
	global_load_ushort v71, v[40:41], off
	global_load_dword v72, v[18:19], off
	v_addc_co_u32_e32 v43, vcc, 0, v13, vcc
	v_add_co_u32_e32 v18, vcc, 0x566dc000, v14
	global_load_ushort v73, v[42:43], off
	s_nop 0
	v_addc_co_u32_e32 v19, vcc, 0, v15, vcc
	v_add_co_u32_e32 v44, vcc, 0x4ea10000, v12
	s_nop 1
	v_addc_co_u32_e32 v45, vcc, 0, v13, vcc
	v_add_co_u32_e32 v46, vcc, 0x566dd000, v14
	global_load_dword v74, v[18:19], off
	global_load_ushort v75, v[44:45], off
	v_addc_co_u32_e32 v47, vcc, 0, v15, vcc
	v_add_co_u32_e32 v18, vcc, 0x4ea50000, v12
	s_nop 1
	v_addc_co_u32_e32 v19, vcc, 0, v13, vcc
	v_add_co_u32_e32 v48, vcc, 0x566de000, v14
	global_load_dword v46, v[46:47], off
	s_nop 0
	global_load_ushort v47, v[18:19], off
	v_addc_co_u32_e32 v49, vcc, 0, v15, vcc
	v_add_co_u32_e32 v12, vcc, 0x4ea90000, v12
	s_nop 1
	v_addc_co_u32_e32 v13, vcc, 0, v13, vcc
	v_add_co_u32_e32 v14, vcc, 0x566df000, v14
	global_load_dword v48, v[48:49], off
	s_nop 0
	global_load_ushort v49, v[12:13], off
	v_addc_co_u32_e32 v15, vcc, 0, v15, vcc
	global_load_dword v14, v[14:15], off
	s_nop 0
	global_store_short_d16_hi v[16:17], v3, off
	s_waitcnt vmcnt(32)
	v_lshlrev_b32_e32 v3, 16, v7
	s_waitcnt vmcnt(31)
	v_fmac_f32_e32 v3, v1, v50
	s_waitcnt vmcnt(30)
	v_lshlrev_b32_e32 v1, 16, v51
	v_bfe_u32 v7, v3, 16, 1
	v_add3_u32 v7, v3, v7, s3
	s_waitcnt vmcnt(29)
	v_fmac_f32_e32 v1, v3, v52
	s_waitcnt vmcnt(28)
	v_lshlrev_b32_e32 v3, 16, v53
	global_store_short_d16_hi v[20:21], v7, off
	v_bfe_u32 v7, v1, 16, 1
	v_add3_u32 v7, v1, v7, s3
	s_waitcnt vmcnt(28)
	v_fmac_f32_e32 v3, v1, v54
	s_waitcnt vmcnt(27)
	v_lshlrev_b32_e32 v1, 16, v55
	global_store_short_d16_hi v[22:23], v7, off
	v_bfe_u32 v7, v3, 16, 1
	v_add3_u32 v7, v3, v7, s3
	s_waitcnt vmcnt(27)
	v_fmac_f32_e32 v1, v3, v56
	s_waitcnt vmcnt(26)
	v_lshlrev_b32_e32 v3, 16, v57
	global_store_short_d16_hi v[24:25], v7, off
	v_bfe_u32 v7, v1, 16, 1
	v_add3_u32 v7, v1, v7, s3
	s_waitcnt vmcnt(26)
	v_fmac_f32_e32 v3, v1, v58
	s_waitcnt vmcnt(25)
	v_lshlrev_b32_e32 v1, 16, v59
	global_store_short_d16_hi v[26:27], v7, off
	v_bfe_u32 v7, v3, 16, 1
	v_add3_u32 v7, v3, v7, s3
	s_waitcnt vmcnt(25)
	v_fmac_f32_e32 v1, v3, v60
	s_waitcnt vmcnt(24)
	v_lshlrev_b32_e32 v3, 16, v61
	global_store_short_d16_hi v[28:29], v7, off
	v_bfe_u32 v7, v1, 16, 1
	v_add3_u32 v7, v1, v7, s3
	s_waitcnt vmcnt(24)
	v_fmac_f32_e32 v3, v1, v62
	s_waitcnt vmcnt(23)
	v_lshlrev_b32_e32 v1, 16, v63
	global_store_short_d16_hi v[30:31], v7, off
	v_bfe_u32 v7, v3, 16, 1
	v_add3_u32 v7, v3, v7, s3
	s_waitcnt vmcnt(23)
	v_fmac_f32_e32 v1, v3, v64
	s_waitcnt vmcnt(22)
	v_lshlrev_b32_e32 v3, 16, v65
	global_store_short_d16_hi v[32:33], v7, off
	v_bfe_u32 v7, v1, 16, 1
	v_add3_u32 v7, v1, v7, s3
	s_waitcnt vmcnt(22)
	v_fmac_f32_e32 v3, v1, v66
	s_waitcnt vmcnt(21)
	v_lshlrev_b32_e32 v1, 16, v67
	global_store_short_d16_hi v[34:35], v7, off
	v_bfe_u32 v7, v3, 16, 1
	v_add3_u32 v7, v3, v7, s3
	s_waitcnt vmcnt(21)
	v_fmac_f32_e32 v1, v3, v68
	s_waitcnt vmcnt(20)
	v_lshlrev_b32_e32 v3, 16, v69
	global_store_short_d16_hi v[36:37], v7, off
	v_bfe_u32 v7, v1, 16, 1
	v_add3_u32 v7, v1, v7, s3
	s_waitcnt vmcnt(20)
	v_fmac_f32_e32 v3, v1, v70
	s_waitcnt vmcnt(19)
	v_lshlrev_b32_e32 v1, 16, v71
	global_store_short_d16_hi v[38:39], v7, off
	v_bfe_u32 v7, v3, 16, 1
	v_add3_u32 v7, v3, v7, s3
	s_waitcnt vmcnt(19)
	v_fmac_f32_e32 v1, v3, v72
	s_waitcnt vmcnt(18)
	v_lshlrev_b32_e32 v3, 16, v73
	global_store_short_d16_hi v[40:41], v7, off
	v_bfe_u32 v7, v1, 16, 1
	v_add3_u32 v7, v1, v7, s3
	s_waitcnt vmcnt(18)
	v_fmac_f32_e32 v3, v1, v74
	s_waitcnt vmcnt(17)
	v_lshlrev_b32_e32 v1, 16, v75
	global_store_short_d16_hi v[42:43], v7, off
	v_bfe_u32 v7, v3, 16, 1
	v_add3_u32 v7, v3, v7, s3
	s_waitcnt vmcnt(17)
	v_fmac_f32_e32 v1, v3, v46
	s_waitcnt vmcnt(16)
	v_lshlrev_b32_e32 v3, 16, v47
	global_store_short_d16_hi v[44:45], v7, off
	v_bfe_u32 v7, v1, 16, 1
	v_add3_u32 v7, v1, v7, s3
	global_store_short_d16_hi v[18:19], v7, off
	s_waitcnt vmcnt(17)
	v_fmac_f32_e32 v3, v1, v48
	s_waitcnt vmcnt(16)
	v_lshlrev_b32_e32 v1, 16, v49
	v_bfe_u32 v7, v3, 16, 1
	v_add3_u32 v7, v3, v7, s3
	s_waitcnt vmcnt(15)
	v_fmac_f32_e32 v1, v3, v14
	global_store_short_d16_hi v[12:13], v7, off
	s_cbranch_scc0 .LBB0_394
	v_add_u32_e32 v2, s6, v2
	v_cmp_lt_i32_e32 vcc, s7, v2
	s_or_b64 s[12:13], vcc, s[12:13]
	v_lshl_add_u64 v[4:5], v[4:5], 0, s[10:11]
	s_andn2_b64 exec, exec, s[12:13]
	s_cbranch_execnz .LBB0_393

.LBB0_2219:
	s_add_u32 s14, s50, s6
	s_addc_u32 s15, s51, s7
	global_load_dwordx4 v[2:5], v[44:45], off
	global_load_dwordx4 v[6:9], v[44:45], off offset:1024
	global_load_dwordx4 v[10:13], v[44:45], off offset:2048
	global_load_dwordx4 v[14:17], v[44:45], off offset:3072
	global_load_dwordx4 v[18:21], v[48:49], off
	global_load_dwordx4 v[22:25], v[50:51], off
	global_load_dwordx4 v[26:29], v[52:53], off
	global_load_dwordx4 v[30:33], v[54:55], off
	global_load_dwordx4 v[34:37], v[46:47], off
	global_load_dwordx4 v[74:77], v73, s[14:15]
	global_load_dwordx4 v[38:41], v1, s[14:15]
	v_add_co_u32_e32 v70, vcc, s3, v64
	v_lshl_add_u64 v[68:69], s[50:51], 0, v[66:67]
	s_nop 0
	v_addc_co_u32_e32 v71, vcc, -1, v65, vcc
	v_add_co_u32_e32 v68, vcc, 0x577d0000, v68
	v_mov_b32_e32 v195, 0
	s_nop 0
	v_addc_co_u32_e32 v69, vcc, 0, v69, vcc
	global_load_dwordx2 v[78:79], v[68:69], off
	global_load_dwordx2 v[80:81], v[68:69], off offset:512
	global_load_dwordx2 v[82:83], v[68:69], off offset:1024
	global_load_dwordx2 v[86:87], v[68:69], off offset:1536
	global_load_dwordx2 v[92:93], v[68:69], off offset:2048
	global_load_dwordx2 v[94:95], v[68:69], off offset:2560
	global_load_dwordx2 v[96:97], v[68:69], off offset:3072
	global_load_dwordx2 v[98:99], v[68:69], off offset:3584
	v_mov_b32_e32 v236, 0
	s_add_i32 s0, s0, s4
	s_add_u32 s6, s6, s8
	s_addc_u32 s7, s7, s9
	v_lshl_add_u64 v[66:67], v[66:67], 0, s[12:13]
	s_cmpk_lt_i32 s0, 0x4000
	s_waitcnt vmcnt(9)
	v_ashrrev_i32_e32 v101, 31, v74
	v_mov_b32_e32 v100, v74
	v_ashrrev_i32_e32 v103, 31, v75
	v_mov_b32_e32 v102, v75
	v_ashrrev_i32_e32 v105, 31, v76
	v_mov_b32_e32 v104, v76
	v_ashrrev_i32_e32 v107, 31, v77
	v_mov_b32_e32 v106, v77
	v_lshlrev_b64 v[102:103], 12, v[102:103]
	v_lshlrev_b64 v[100:101], 12, v[100:101]
	v_lshlrev_b64 v[106:107], 12, v[106:107]
	v_lshlrev_b64 v[104:105], 12, v[104:105]
	v_lshl_add_u64 v[100:101], v[42:43], 0, v[100:101]
	v_lshl_add_u64 v[102:103], v[42:43], 0, v[102:103]
	v_lshl_add_u64 v[104:105], v[42:43], 0, v[104:105]
	v_lshl_add_u64 v[106:107], v[42:43], 0, v[106:107]
	global_load_dwordx2 v[114:115], v[100:101], off
	global_load_dwordx2 v[116:117], v[102:103], off
	global_load_dwordx2 v[118:119], v[104:105], off
	global_load_dwordx2 v[120:121], v[106:107], off
	global_load_dwordx2 v[122:123], v[100:101], off offset:512
	global_load_dwordx2 v[124:125], v[102:103], off offset:512
	global_load_dwordx2 v[126:127], v[104:105], off offset:512
	global_load_dwordx2 v[128:129], v[106:107], off offset:512
	global_load_dwordx2 v[130:131], v[100:101], off offset:1024
	global_load_dwordx2 v[132:133], v[102:103], off offset:1024
	global_load_dwordx2 v[134:135], v[104:105], off offset:1024
	global_load_dwordx2 v[136:137], v[106:107], off offset:1024
	global_load_dwordx2 v[138:139], v[100:101], off offset:1536
	global_load_dwordx2 v[140:141], v[102:103], off offset:1536
	global_load_dwordx2 v[142:143], v[104:105], off offset:1536
	global_load_dwordx2 v[144:145], v[106:107], off offset:1536
	global_load_dwordx2 v[146:147], v[100:101], off offset:2048
	global_load_dwordx2 v[148:149], v[102:103], off offset:2048
	global_load_dwordx2 v[150:151], v[104:105], off offset:2048
	global_load_dwordx2 v[152:153], v[100:101], off offset:2560
	global_load_dwordx2 v[154:155], v[100:101], off offset:3072
	s_nop 0
	global_load_dwordx2 v[100:101], v[100:101], off offset:3584
	s_nop 0
	global_load_dwordx2 v[156:157], v[106:107], off offset:2048
	global_load_dwordx2 v[158:159], v[102:103], off offset:2560
	global_load_dwordx2 v[160:161], v[102:103], off offset:3072
	s_nop 0
	global_load_dwordx2 v[102:103], v[102:103], off offset:3584
	s_nop 0
	global_load_dwordx2 v[162:163], v[104:105], off offset:2560
	global_load_dwordx2 v[164:165], v[104:105], off offset:3072
	s_nop 0
	global_load_dwordx2 v[104:105], v[104:105], off offset:3584
	s_nop 0
	global_load_dwordx2 v[166:167], v[106:107], off offset:2560
	global_load_dwordx2 v[168:169], v[106:107], off offset:3072
	s_nop 0
	global_load_dwordx2 v[106:107], v[106:107], off offset:3584
	s_waitcnt vmcnt(40)
	v_mov_b32_e32 v72, v41
	s_waitcnt vmcnt(39)
	v_lshlrev_b32_e32 v68, 16, v78
	v_and_b32_e32 v69, 0xffff0000, v78
	v_lshlrev_b32_e32 v76, 16, v79
	v_and_b32_e32 v77, 0xffff0000, v79
	s_waitcnt vmcnt(38)
	v_lshlrev_b32_e32 v74, 16, v80
	v_and_b32_e32 v75, 0xffff0000, v80
	v_lshlrev_b32_e32 v80, 16, v81
	v_and_b32_e32 v81, 0xffff0000, v81
	s_waitcnt vmcnt(37)
	v_lshlrev_b32_e32 v78, 16, v82
	v_and_b32_e32 v79, 0xffff0000, v82
	v_lshlrev_b32_e32 v84, 16, v83
	v_and_b32_e32 v85, 0xffff0000, v83
	s_waitcnt vmcnt(32)
	v_lshlrev_b32_e32 v112, 16, v98
	v_and_b32_e32 v113, 0xffff0000, v98
	v_lshlrev_b32_e32 v98, 16, v99
	v_and_b32_e32 v99, 0xffff0000, v99
	v_lshlrev_b32_e32 v82, 16, v86
	v_and_b32_e32 v83, 0xffff0000, v86
	v_lshlrev_b32_e32 v88, 16, v87
	v_and_b32_e32 v89, 0xffff0000, v87
	v_lshlrev_b32_e32 v86, 16, v92
	v_and_b32_e32 v87, 0xffff0000, v92
	v_lshlrev_b32_e32 v92, 16, v93
	v_and_b32_e32 v93, 0xffff0000, v93
	v_lshlrev_b32_e32 v108, 16, v94
	v_and_b32_e32 v109, 0xffff0000, v94
	v_lshlrev_b32_e32 v94, 16, v95
	v_and_b32_e32 v95, 0xffff0000, v95
	v_lshlrev_b32_e32 v110, 16, v96
	v_and_b32_e32 v111, 0xffff0000, v96
	v_lshlrev_b32_e32 v96, 16, v97
	v_and_b32_e32 v97, 0xffff0000, v97
	s_waitcnt vmcnt(31)
	v_lshlrev_b32_e32 v170, 16, v114
	v_and_b32_e32 v171, 0xffff0000, v114
	v_lshlrev_b32_e32 v114, 16, v115
	v_and_b32_e32 v115, 0xffff0000, v115
	s_waitcnt vmcnt(27)
	v_lshlrev_b32_e32 v178, 16, v122
	v_and_b32_e32 v179, 0xffff0000, v122
	v_lshlrev_b32_e32 v122, 16, v123
	v_and_b32_e32 v123, 0xffff0000, v123
	v_lshlrev_b32_e32 v172, 16, v116
	v_and_b32_e32 v173, 0xffff0000, v116
	v_lshlrev_b32_e32 v116, 16, v117
	v_and_b32_e32 v117, 0xffff0000, v117
	s_waitcnt vmcnt(26)
	v_lshlrev_b32_e32 v180, 16, v124
	v_and_b32_e32 v181, 0xffff0000, v124
	v_lshlrev_b32_e32 v124, 16, v125
	v_and_b32_e32 v125, 0xffff0000, v125
	s_waitcnt vmcnt(23)
	v_lshlrev_b32_e32 v186, 16, v130
	v_and_b32_e32 v187, 0xffff0000, v130
	v_lshlrev_b32_e32 v130, 16, v131
	v_and_b32_e32 v131, 0xffff0000, v131
	s_waitcnt vmcnt(19)
	v_lshlrev_b32_e32 v196, 16, v138
	v_and_b32_e32 v197, 0xffff0000, v138
	v_lshlrev_b32_e32 v138, 16, v139
	v_and_b32_e32 v139, 0xffff0000, v139
	s_waitcnt vmcnt(15)
	v_lshlrev_b32_e32 v204, 16, v146
	v_and_b32_e32 v205, 0xffff0000, v146
	v_lshlrev_b32_e32 v146, 16, v147
	v_and_b32_e32 v147, 0xffff0000, v147
	s_waitcnt vmcnt(12)
	v_lshlrev_b32_e32 v212, 16, v152
	v_and_b32_e32 v213, 0xffff0000, v152
	v_lshlrev_b32_e32 v152, 16, v153
	v_and_b32_e32 v153, 0xffff0000, v153
	s_waitcnt vmcnt(11)
	v_lshlrev_b32_e32 v220, 16, v154
	v_and_b32_e32 v221, 0xffff0000, v154
	v_lshlrev_b32_e32 v154, 16, v155
	v_and_b32_e32 v155, 0xffff0000, v155
	s_waitcnt vmcnt(10)
	v_lshlrev_b32_e32 v228, 16, v100
	v_and_b32_e32 v229, 0xffff0000, v100
	v_lshlrev_b32_e32 v100, 16, v101
	v_and_b32_e32 v101, 0xffff0000, v101
	v_pk_fma_f32 v[170:171], v[38:39], v[170:171], 0 op_sel_hi:[0,1,0]
	v_pk_fma_f32 v[114:115], v[38:39], v[114:115], 0 op_sel_hi:[0,1,0]
	v_pk_fma_f32 v[178:179], v[38:39], v[178:179], 0 op_sel_hi:[0,1,0]
	v_pk_fma_f32 v[122:123], v[38:39], v[122:123], 0 op_sel_hi:[0,1,0]
	v_lshlrev_b32_e32 v174, 16, v118
	v_and_b32_e32 v175, 0xffff0000, v118
	v_lshlrev_b32_e32 v118, 16, v119
	v_and_b32_e32 v119, 0xffff0000, v119
	v_lshlrev_b32_e32 v182, 16, v126
	v_and_b32_e32 v183, 0xffff0000, v126
	v_lshlrev_b32_e32 v126, 16, v127
	v_and_b32_e32 v127, 0xffff0000, v127
	v_lshlrev_b32_e32 v188, 16, v132
	v_and_b32_e32 v189, 0xffff0000, v132
	v_lshlrev_b32_e32 v132, 16, v133
	v_and_b32_e32 v133, 0xffff0000, v133
	v_lshlrev_b32_e32 v198, 16, v140
	v_and_b32_e32 v199, 0xffff0000, v140
	v_lshlrev_b32_e32 v140, 16, v141
	v_and_b32_e32 v141, 0xffff0000, v141
	v_lshlrev_b32_e32 v206, 16, v148
	v_and_b32_e32 v207, 0xffff0000, v148
	v_lshlrev_b32_e32 v148, 16, v149
	v_and_b32_e32 v149, 0xffff0000, v149
	s_waitcnt vmcnt(8)
	v_lshlrev_b32_e32 v214, 16, v158
	v_and_b32_e32 v215, 0xffff0000, v158
	v_lshlrev_b32_e32 v158, 16, v159
	v_and_b32_e32 v159, 0xffff0000, v159
	s_waitcnt vmcnt(7)
	v_lshlrev_b32_e32 v222, 16, v160
	v_and_b32_e32 v223, 0xffff0000, v160
	v_lshlrev_b32_e32 v160, 16, v161
	v_and_b32_e32 v161, 0xffff0000, v161
	s_waitcnt vmcnt(6)
	v_lshlrev_b32_e32 v230, 16, v102
	v_and_b32_e32 v231, 0xffff0000, v102
	v_lshlrev_b32_e32 v102, 16, v103
	v_and_b32_e32 v103, 0xffff0000, v103
	v_pk_fma_f32 v[186:187], v[38:39], v[186:187], 0 op_sel_hi:[0,1,0]
	v_pk_fma_f32 v[130:131], v[38:39], v[130:131], 0 op_sel_hi:[0,1,0]
	v_pk_fma_f32 v[196:197], v[38:39], v[196:197], 0 op_sel_hi:[0,1,0]
	v_pk_fma_f32 v[138:139], v[38:39], v[138:139], 0 op_sel_hi:[0,1,0]
	v_pk_fma_f32 v[204:205], v[38:39], v[204:205], 0 op_sel_hi:[0,1,0]
	v_pk_fma_f32 v[146:147], v[38:39], v[146:147], 0 op_sel_hi:[0,1,0]
	v_pk_fma_f32 v[212:213], v[38:39], v[212:213], 0 op_sel_hi:[0,1,0]
	v_pk_fma_f32 v[152:153], v[38:39], v[152:153], 0 op_sel_hi:[0,1,0]
	v_pk_fma_f32 v[220:221], v[38:39], v[220:221], 0 op_sel_hi:[0,1,0]
	v_pk_fma_f32 v[154:155], v[38:39], v[154:155], 0 op_sel_hi:[0,1,0]
	v_pk_fma_f32 v[228:229], v[38:39], v[228:229], 0 op_sel_hi:[0,1,0]
	v_pk_fma_f32 v[100:101], v[38:39], v[100:101], 0 op_sel_hi:[0,1,0]
	v_pk_fma_f32 v[170:171], v[38:39], v[172:173], v[170:171] op_sel:[1,0,0]
	v_pk_fma_f32 v[114:115], v[38:39], v[116:117], v[114:115] op_sel:[1,0,0]
	v_pk_fma_f32 v[116:117], v[38:39], v[180:181], v[178:179] op_sel:[1,0,0]
	v_pk_fma_f32 v[122:123], v[38:39], v[124:125], v[122:123] op_sel:[1,0,0]
	v_lshlrev_b32_e32 v176, 16, v120
	v_and_b32_e32 v177, 0xffff0000, v120
	v_lshlrev_b32_e32 v120, 16, v121
	v_and_b32_e32 v121, 0xffff0000, v121
	v_lshlrev_b32_e32 v184, 16, v128
	v_and_b32_e32 v185, 0xffff0000, v128
	v_lshlrev_b32_e32 v128, 16, v129
	v_and_b32_e32 v129, 0xffff0000, v129
	v_lshlrev_b32_e32 v190, 16, v134
	v_and_b32_e32 v191, 0xffff0000, v134
	v_lshlrev_b32_e32 v134, 16, v135
	v_and_b32_e32 v135, 0xffff0000, v135
	v_lshlrev_b32_e32 v200, 16, v142
	v_and_b32_e32 v201, 0xffff0000, v142
	v_lshlrev_b32_e32 v142, 16, v143
	v_and_b32_e32 v143, 0xffff0000, v143
	v_lshlrev_b32_e32 v208, 16, v150
	v_and_b32_e32 v209, 0xffff0000, v150
	v_lshlrev_b32_e32 v150, 16, v151
	v_and_b32_e32 v151, 0xffff0000, v151
	s_waitcnt vmcnt(5)
	v_lshlrev_b32_e32 v216, 16, v162
	v_and_b32_e32 v217, 0xffff0000, v162
	v_lshlrev_b32_e32 v162, 16, v163
	v_and_b32_e32 v163, 0xffff0000, v163
	s_waitcnt vmcnt(4)
	v_lshlrev_b32_e32 v224, 16, v164
	v_and_b32_e32 v225, 0xffff0000, v164
	v_lshlrev_b32_e32 v164, 16, v165
	v_and_b32_e32 v165, 0xffff0000, v165
	s_waitcnt vmcnt(3)
	v_lshlrev_b32_e32 v232, 16, v104
	v_and_b32_e32 v233, 0xffff0000, v104
	v_lshlrev_b32_e32 v104, 16, v105
	v_and_b32_e32 v105, 0xffff0000, v105
	v_pk_fma_f32 v[124:125], v[38:39], v[188:189], v[186:187] op_sel:[1,0,0]
	v_pk_fma_f32 v[130:131], v[38:39], v[132:133], v[130:131] op_sel:[1,0,0]
	v_pk_fma_f32 v[132:133], v[38:39], v[198:199], v[196:197] op_sel:[1,0,0]
	v_pk_fma_f32 v[138:139], v[38:39], v[140:141], v[138:139] op_sel:[1,0,0]
	v_pk_fma_f32 v[140:141], v[38:39], v[206:207], v[204:205] op_sel:[1,0,0]
	v_pk_fma_f32 v[146:147], v[38:39], v[148:149], v[146:147] op_sel:[1,0,0]
	v_pk_fma_f32 v[148:149], v[38:39], v[214:215], v[212:213] op_sel:[1,0,0]
	v_pk_fma_f32 v[152:153], v[38:39], v[158:159], v[152:153] op_sel:[1,0,0]
	v_pk_fma_f32 v[158:159], v[38:39], v[222:223], v[220:221] op_sel:[1,0,0]
	v_pk_fma_f32 v[154:155], v[38:39], v[160:161], v[154:155] op_sel:[1,0,0]
	v_pk_fma_f32 v[160:161], v[38:39], v[230:231], v[228:229] op_sel:[1,0,0]
	v_pk_fma_f32 v[38:39], v[38:39], v[102:103], v[100:101] op_sel:[1,0,0]
	v_pk_fma_f32 v[100:101], v[40:41], v[174:175], v[170:171] op_sel_hi:[0,1,1]
	v_pk_fma_f32 v[102:103], v[40:41], v[118:119], v[114:115] op_sel_hi:[0,1,1]
	v_pk_fma_f32 v[114:115], v[40:41], v[182:183], v[116:117] op_sel_hi:[0,1,1]
	v_pk_fma_f32 v[116:117], v[40:41], v[126:127], v[122:123] op_sel_hi:[0,1,1]
	v_lshlrev_b32_e32 v192, 16, v136
	v_and_b32_e32 v193, 0xffff0000, v136
	v_lshlrev_b32_e32 v136, 16, v137
	v_and_b32_e32 v137, 0xffff0000, v137
	v_pk_fma_f32 v[118:119], v[40:41], v[190:191], v[124:125] op_sel_hi:[0,1,1]
	v_pk_fma_f32 v[122:123], v[40:41], v[134:135], v[130:131] op_sel_hi:[0,1,1]
	v_pk_fma_f32 v[124:125], v[40:41], v[200:201], v[132:133] op_sel_hi:[0,1,1]
	v_pk_fma_f32 v[126:127], v[40:41], v[142:143], v[138:139] op_sel_hi:[0,1,1]
	v_pk_fma_f32 v[130:131], v[40:41], v[208:209], v[140:141] op_sel_hi:[0,1,1]
	v_pk_fma_f32 v[132:133], v[40:41], v[150:151], v[146:147] op_sel_hi:[0,1,1]
	v_pk_fma_f32 v[134:135], v[40:41], v[216:217], v[148:149] op_sel_hi:[0,1,1]
	v_pk_fma_f32 v[138:139], v[40:41], v[162:163], v[152:153] op_sel_hi:[0,1,1]
	v_pk_fma_f32 v[140:141], v[40:41], v[224:225], v[158:159] op_sel_hi:[0,1,1]
	v_pk_fma_f32 v[142:143], v[40:41], v[164:165], v[154:155] op_sel_hi:[0,1,1]
	v_pk_fma_f32 v[146:147], v[40:41], v[232:233], v[160:161] op_sel_hi:[0,1,1]
	v_pk_fma_f32 v[38:39], v[40:41], v[104:105], v[38:39] op_sel_hi:[0,1,1]
	v_pk_fma_f32 v[40:41], v[72:73], v[176:177], v[100:101] op_sel_hi:[0,1,1]
	v_pk_fma_f32 v[100:101], v[72:73], v[120:121], v[102:103] op_sel_hi:[0,1,1]
	v_pk_fma_f32 v[102:103], v[72:73], v[184:185], v[114:115] op_sel_hi:[0,1,1]
	v_pk_fma_f32 v[104:105], v[72:73], v[128:129], v[116:117] op_sel_hi:[0,1,1]
	s_waitcnt vmcnt(0)
	v_lshlrev_b32_e32 v234, 16, v106
	v_and_b32_e32 v235, 0xffff0000, v106
	v_lshlrev_b32_e32 v106, 16, v107
	v_and_b32_e32 v107, 0xffff0000, v107
	v_pk_fma_f32 v[114:115], v[72:73], v[192:193], v[118:119] op_sel_hi:[0,1,1]
	v_pk_fma_f32 v[116:117], v[72:73], v[136:137], v[122:123] op_sel_hi:[0,1,1]
	v_pk_fma_f32 v[4:5], v[100:101], v[4:5], v[76:77]
	v_pk_fma_f32 v[2:3], v[40:41], v[2:3], v[68:69]
	v_pk_fma_f32 v[8:9], v[104:105], v[8:9], v[80:81]
	v_pk_fma_f32 v[6:7], v[102:103], v[6:7], v[74:75]
	v_lshlrev_b32_e32 v202, 16, v144
	v_and_b32_e32 v203, 0xffff0000, v144
	v_lshlrev_b32_e32 v144, 16, v145
	v_and_b32_e32 v145, 0xffff0000, v145
	v_lshlrev_b32_e32 v210, 16, v156
	v_and_b32_e32 v211, 0xffff0000, v156
	v_lshlrev_b32_e32 v156, 16, v157
	v_and_b32_e32 v157, 0xffff0000, v157
	v_pk_fma_f32 v[38:39], v[72:73], v[106:107], v[38:39] op_sel_hi:[0,1,1]
	v_pk_fma_f32 v[10:11], v[114:115], v[10:11], v[78:79]
	v_pk_fma_f32 v[12:13], v[116:117], v[12:13], v[84:85]
	v_mov_b32_e32 v40, v3
	v_mov_b32_e32 v41, v7
	v_mov_b32_e32 v74, v5
	v_mov_b32_e32 v75, v9
	v_pk_fma_f32 v[118:119], v[72:73], v[202:203], v[124:125] op_sel_hi:[0,1,1]
	v_pk_fma_f32 v[120:121], v[72:73], v[144:145], v[126:127] op_sel_hi:[0,1,1]
	v_pk_fma_f32 v[124:125], v[72:73], v[156:157], v[132:133] op_sel_hi:[0,1,1]
	v_pk_fma_f32 v[32:33], v[38:39], v[32:33], v[98:99]
	v_mov_b32_e32 v38, v2
	v_mov_b32_e32 v39, v6
	v_mov_b32_e32 v68, v4
	v_mov_b32_e32 v69, v8
	v_pk_mul_f32 v[76:77], v[12:13], v[12:13]
	v_pk_mul_f32 v[78:79], v[10:11], v[10:11]
	v_pk_mul_f32 v[40:41], v[40:41], v[40:41]
	v_pk_mul_f32 v[74:75], v[74:75], v[74:75]
	v_lshlrev_b32_e32 v218, 16, v166
	v_and_b32_e32 v219, 0xffff0000, v166
	v_lshlrev_b32_e32 v166, 16, v167
	v_and_b32_e32 v167, 0xffff0000, v167
	v_lshlrev_b32_e32 v226, 16, v168
	v_and_b32_e32 v227, 0xffff0000, v168
	v_lshlrev_b32_e32 v168, 16, v169
	v_and_b32_e32 v169, 0xffff0000, v169
	v_pk_fma_f32 v[122:123], v[72:73], v[210:211], v[130:131] op_sel_hi:[0,1,1]
	v_pk_fma_f32 v[16:17], v[120:121], v[16:17], v[88:89]
	v_pk_fma_f32 v[14:15], v[118:119], v[14:15], v[82:83]
	v_pk_fma_f32 v[20:21], v[124:125], v[20:21], v[92:93]
	v_pk_mov_b32 v[92:93], v[78:79], v[76:77] op_sel:[1,0]
	v_mov_b32_e32 v79, v77
	v_pk_fma_f32 v[38:39], v[38:39], v[38:39], v[40:41]
	v_pk_fma_f32 v[40:41], v[68:69], v[68:69], v[74:75]
	v_pk_fma_f32 v[126:127], v[72:73], v[218:219], v[134:135] op_sel_hi:[0,1,1]
	v_pk_fma_f32 v[128:129], v[72:73], v[166:167], v[138:139] op_sel_hi:[0,1,1]
	v_pk_fma_f32 v[130:131], v[72:73], v[226:227], v[140:141] op_sel_hi:[0,1,1]
	v_pk_fma_f32 v[132:133], v[72:73], v[168:169], v[142:143] op_sel_hi:[0,1,1]
	v_pk_fma_f32 v[134:135], v[72:73], v[234:235], v[146:147] op_sel_hi:[0,1,1]
	v_pk_fma_f32 v[18:19], v[122:123], v[18:19], v[86:87]
	v_mul_f32_e32 v72, v15, v15
	v_mul_f32_e32 v80, v17, v17
	v_pk_add_f32 v[68:69], v[92:93], v[78:79]
	v_pk_add_f32 v[38:39], v[38:39], v[40:41]
	v_pk_fma_f32 v[22:23], v[126:127], v[22:23], v[108:109]
	v_pk_fma_f32 v[24:25], v[128:129], v[24:25], v[94:95]
	v_pk_fma_f32 v[28:29], v[132:133], v[28:29], v[96:97]
	v_mul_f32_e32 v89, v18, v18
	v_mul_f32_e32 v96, v19, v19
	v_mul_f32_e32 v97, v20, v20
	v_mul_f32_e32 v98, v21, v21
	v_pk_fma_f32 v[76:77], v[14:15], v[14:15], v[72:73] op_sel_hi:[1,1,0]
	v_pk_fma_f32 v[80:81], v[16:17], v[16:17], v[80:81] op_sel_hi:[1,1,0]
	v_pk_add_f32 v[40:41], v[68:69], v[68:69] op_sel:[0,1] op_sel_hi:[1,0]
	v_pk_add_f32 v[38:39], v[38:39], v[38:39] op_sel:[0,1] op_sel_hi:[1,0]
	v_pk_mul_f32 v[82:83], v[24:25], v[24:25]
	v_pk_mul_f32 v[84:85], v[22:23], v[22:23]
	v_mov_b32_e32 v77, v97
	v_mov_b32_e32 v81, v98
	v_mov_b32_e32 v41, v96
	v_mov_b32_e32 v39, v89
	v_pk_fma_f32 v[26:27], v[130:131], v[26:27], v[110:111]
	v_pk_mov_b32 v[94:95], v[84:85], v[82:83] op_sel:[1,0]
	v_mov_b32_e32 v85, v83
	v_pk_add_f32 v[68:69], v[76:77], v[80:81]
	v_pk_add_f32 v[38:39], v[38:39], v[40:41]
	v_pk_fma_f32 v[30:31], v[134:135], v[30:31], v[112:113]
	v_mul_f32_e32 v86, v27, v27
	v_mul_f32_e32 v88, v29, v29
	v_pk_add_f32 v[74:75], v[94:95], v[84:85]
	v_pk_add_f32 v[38:39], v[38:39], v[68:69]
	v_mul_f32_e32 v99, v30, v30
	v_mul_f32_e32 v100, v31, v31
	v_mul_f32_e32 v101, v32, v32
	v_mul_f32_e32 v102, v33, v33
	v_pk_fma_f32 v[82:83], v[26:27], v[26:27], v[86:87] op_sel_hi:[1,1,0]
	v_pk_fma_f32 v[86:87], v[28:29], v[28:29], v[88:89] op_sel_hi:[1,1,0]
	v_pk_add_f32 v[74:75], v[74:75], v[74:75] op_sel:[0,1] op_sel_hi:[1,0]
	v_pk_add_f32 v[38:39], v[38:39], v[38:39] op_sel:[0,1] op_sel_hi:[1,0]
	v_mov_b32_e32 v83, v101
	v_mov_b32_e32 v87, v102
	v_mov_b32_e32 v75, v100
	v_mov_b32_e32 v39, v99
	v_pk_add_f32 v[76:77], v[82:83], v[86:87]
	global_load_dwordx4 v[100:103], v[46:47], off offset:1024
	global_load_dwordx4 v[104:107], v[46:47], off offset:2048
	global_load_dwordx4 v[108:111], v[46:47], off offset:3072
	global_load_dwordx4 v[112:115], v[56:57], off
	global_load_dwordx4 v[116:119], v[58:59], off
	global_load_dwordx4 v[120:123], v[60:61], off
	global_load_dwordx4 v[124:127], v[62:63], off
	v_pk_add_f32 v[38:39], v[38:39], v[74:75]
	s_nop 0
	v_pk_add_f32 v[38:39], v[38:39], v[76:77]
	s_nop 0
	v_add_f32_e32 v38, v38, v39
	s_nop 1
	v_add_f32_dpp v38, v38, v38 row_shr:1 row_mask:0xf bank_mask:0xf bound_ctrl:1
	s_nop 1
	v_add_f32_dpp v38, v38, v38 row_shr:2 row_mask:0xf bank_mask:0xf bound_ctrl:1
	s_nop 1
	v_add_f32_dpp v38, v38, v38 row_shr:4 row_mask:0xf bank_mask:0xf bound_ctrl:1
	s_nop 1
	v_add_f32_dpp v38, v38, v38 row_shr:8 row_mask:0xf bank_mask:0xf bound_ctrl:1
	s_nop 1
	v_mov_b32_dpp v195, v38 row_bcast:15 row_mask:0xa bank_mask:0xf
	v_add_f32_e32 v38, v38, v195
	s_nop 1
	v_mov_b32_dpp v236, v38 row_bcast:31 row_mask:0xc bank_mask:0xf
	v_add_f32_e32 v38, v38, v236
	s_nop 0
	v_readlane_b32 s5, v38, 63
	s_nop 1
	v_fma_f32 v38, s5, v91, v90
	v_mul_f32_e32 v39, 0x4b800000, v38
	v_cmp_gt_f32_e32 vcc, s1, v38
	s_nop 1
	v_cndmask_b32_e32 v38, v38, v39, vcc
	v_rsq_f32_e32 v38, v38
	s_nop 0
	v_mul_f32_e32 v39, 0x45800000, v38
	v_cndmask_b32_e32 v38, v38, v39, vcc
	v_pk_mul_f32 v[2:3], v[38:39], v[2:3] op_sel_hi:[0,1]
	v_pk_mul_f32 v[4:5], v[38:39], v[4:5] op_sel_hi:[0,1]
	v_pk_mul_f32 v[4:5], v[36:37], v[4:5]
	v_pk_mul_f32 v[2:3], v[34:35], v[2:3]
	global_store_dwordx4 v[70:71], v[2:5], off offset:-3072
	v_pk_mul_f32 v[8:9], v[38:39], v[8:9] op_sel_hi:[0,1]
	v_pk_mul_f32 v[6:7], v[38:39], v[6:7] op_sel_hi:[0,1]
	s_waitcnt vmcnt(7)
	v_pk_mul_f32 v[2:3], v[100:101], v[6:7]
	v_pk_mul_f32 v[4:5], v[102:103], v[8:9]
	global_store_dwordx4 v[70:71], v[2:5], off offset:-2048
	v_pk_mul_f32 v[6:7], v[38:39], v[12:13] op_sel_hi:[0,1]
	v_pk_mul_f32 v[8:9], v[38:39], v[10:11] op_sel_hi:[0,1]
	s_waitcnt vmcnt(7)
	v_pk_mul_f32 v[2:3], v[104:105], v[8:9]
	v_pk_mul_f32 v[4:5], v[106:107], v[6:7]
	global_store_dwordx4 v[70:71], v[2:5], off offset:-1024
	v_pk_mul_f32 v[6:7], v[38:39], v[16:17] op_sel_hi:[0,1]
	v_pk_mul_f32 v[8:9], v[38:39], v[14:15] op_sel_hi:[0,1]
	s_waitcnt vmcnt(7)
	v_pk_mul_f32 v[2:3], v[108:109], v[8:9]
	v_pk_mul_f32 v[4:5], v[110:111], v[6:7]
	global_store_dwordx4 v[64:65], v[2:5], off offset:-4096
	v_pk_mul_f32 v[6:7], v[38:39], v[20:21] op_sel_hi:[0,1]
	v_pk_mul_f32 v[8:9], v[38:39], v[18:19] op_sel_hi:[0,1]
	s_waitcnt vmcnt(7)
	v_pk_mul_f32 v[2:3], v[112:113], v[8:9]
	v_pk_mul_f32 v[4:5], v[114:115], v[6:7]
	global_store_dwordx4 v[64:65], v[2:5], off offset:-3072
	v_pk_mul_f32 v[6:7], v[38:39], v[24:25] op_sel_hi:[0,1]
	v_pk_mul_f32 v[8:9], v[38:39], v[22:23] op_sel_hi:[0,1]
	s_waitcnt vmcnt(7)
	v_pk_mul_f32 v[2:3], v[116:117], v[8:9]
	v_pk_mul_f32 v[4:5], v[118:119], v[6:7]
	global_store_dwordx4 v[64:65], v[2:5], off offset:-2048
	v_pk_mul_f32 v[6:7], v[38:39], v[28:29] op_sel_hi:[0,1]
	v_pk_mul_f32 v[8:9], v[38:39], v[26:27] op_sel_hi:[0,1]
	s_waitcnt vmcnt(7)
	v_pk_mul_f32 v[2:3], v[120:121], v[8:9]
	v_pk_mul_f32 v[4:5], v[122:123], v[6:7]
	global_store_dwordx4 v[64:65], v[2:5], off offset:-1024
	v_pk_mul_f32 v[6:7], v[38:39], v[32:33] op_sel_hi:[0,1]
	v_pk_mul_f32 v[8:9], v[38:39], v[30:31] op_sel_hi:[0,1]
	s_waitcnt vmcnt(7)
	v_pk_mul_f32 v[2:3], v[124:125], v[8:9]
	v_pk_mul_f32 v[4:5], v[126:127], v[6:7]
	global_store_dwordx4 v[64:65], v[2:5], off
	v_lshl_add_u64 v[64:65], v[64:65], 0, s[10:11]
	s_cbranch_scc1 .LBB0_2219
